# P0 fp8 weight transposes: 8 dwordx4 loads per item in batches of 2 (was 32 dword loads, 16 in flight), conflict-free LDS writes
# speedup vs baseline: 1.0162x; 1.0080x over previous
.LBB0_16:
	v_readfirstlane_b32 s50, v18
	s_lshl_b32 s51, s8, 12
	s_lshl_b32 s50, s50, 2
	s_add_u32 s50, s50, s51
	s_add_u32 s56, s6, s50
	s_addc_u32 s57, s7, 0
	v_and_b32_e32 v100, 3, v36
	v_lshrrev_b32_e32 v101, 5, v36
	v_lshl_or_b32 v100, v101, 2, v100
	v_bfe_u32 v101, v36, 2, 3
	v_lshlrev_b32_e32 v102, 12, v100
	v_lshl_or_b32 v102, v101, 4, v102
	v_lshlrev_b32_e32 v103, 2, v6
	v_sub_u32_e32 v103, v8, v103
	v_mad_u32_u24 v103, v100, s15, v103
	v_lshl_add_u32 v103, v101, 4, v103
	global_load_dwordx4 v[120:123], v102, s[56:57]
	s_add_u32 s56, s56, 0x8000
	s_addc_u32 s57, s57, 0
	global_load_dwordx4 v[124:127], v102, s[56:57]
	s_add_u32 s56, s56, 0x8000
	s_addc_u32 s57, s57, 0
	s_waitcnt vmcnt(1)
	v_pk_mul_f32 v[120:121], v[120:121], s[10:11] op_sel_hi:[1,0]
	v_pk_mul_f32 v[122:123], v[122:123], s[10:11] op_sel_hi:[1,0]
	ds_write_b32 v103, v120 offset:0
	ds_write_b32 v103, v121 offset:4
	ds_write_b32 v103, v122 offset:8
	ds_write_b32 v103, v123 offset:12
	s_waitcnt vmcnt(0)
	v_pk_mul_f32 v[124:125], v[124:125], s[10:11] op_sel_hi:[1,0]
	v_pk_mul_f32 v[126:127], v[126:127], s[10:11] op_sel_hi:[1,0]
	ds_write_b32 v103, v124 offset:1056
	ds_write_b32 v103, v125 offset:1060
	ds_write_b32 v103, v126 offset:1064
	ds_write_b32 v103, v127 offset:1068
	global_load_dwordx4 v[128:131], v102, s[56:57]
	s_add_u32 s56, s56, 0x8000
	s_addc_u32 s57, s57, 0
	global_load_dwordx4 v[132:135], v102, s[56:57]
	s_add_u32 s56, s56, 0x8000
	s_addc_u32 s57, s57, 0
	s_waitcnt vmcnt(1)
	v_pk_mul_f32 v[128:129], v[128:129], s[10:11] op_sel_hi:[1,0]
	v_pk_mul_f32 v[130:131], v[130:131], s[10:11] op_sel_hi:[1,0]
	ds_write_b32 v103, v128 offset:2112
	ds_write_b32 v103, v129 offset:2116
	ds_write_b32 v103, v130 offset:2120
	ds_write_b32 v103, v131 offset:2124
	s_waitcnt vmcnt(0)
	v_pk_mul_f32 v[132:133], v[132:133], s[10:11] op_sel_hi:[1,0]
	v_pk_mul_f32 v[134:135], v[134:135], s[10:11] op_sel_hi:[1,0]
	ds_write_b32 v103, v132 offset:3168
	ds_write_b32 v103, v133 offset:3172
	ds_write_b32 v103, v134 offset:3176
	ds_write_b32 v103, v135 offset:3180
	global_load_dwordx4 v[136:139], v102, s[56:57]
	s_add_u32 s56, s56, 0x8000
	s_addc_u32 s57, s57, 0
	global_load_dwordx4 v[140:143], v102, s[56:57]
	s_add_u32 s56, s56, 0x8000
	s_addc_u32 s57, s57, 0
	s_waitcnt vmcnt(1)
	v_pk_mul_f32 v[136:137], v[136:137], s[10:11] op_sel_hi:[1,0]
	v_pk_mul_f32 v[138:139], v[138:139], s[10:11] op_sel_hi:[1,0]
	ds_write_b32 v103, v136 offset:4224
	ds_write_b32 v103, v137 offset:4228
	ds_write_b32 v103, v138 offset:4232
	ds_write_b32 v103, v139 offset:4236
	s_waitcnt vmcnt(0)
	v_pk_mul_f32 v[140:141], v[140:141], s[10:11] op_sel_hi:[1,0]
	v_pk_mul_f32 v[142:143], v[142:143], s[10:11] op_sel_hi:[1,0]
	ds_write_b32 v103, v140 offset:5280
	ds_write_b32 v103, v141 offset:5284
	ds_write_b32 v103, v142 offset:5288
	ds_write_b32 v103, v143 offset:5292
	global_load_dwordx4 v[144:147], v102, s[56:57]
	s_add_u32 s56, s56, 0x8000
	s_addc_u32 s57, s57, 0
	global_load_dwordx4 v[148:151], v102, s[56:57]
	s_add_u32 s56, s56, 0x8000
	s_addc_u32 s57, s57, 0
	s_waitcnt vmcnt(1)
	v_pk_mul_f32 v[144:145], v[144:145], s[10:11] op_sel_hi:[1,0]
	v_pk_mul_f32 v[146:147], v[146:147], s[10:11] op_sel_hi:[1,0]
	ds_write_b32 v103, v144 offset:6336
	ds_write_b32 v103, v145 offset:6340
	ds_write_b32 v103, v146 offset:6344
	ds_write_b32 v103, v147 offset:6348
	s_waitcnt vmcnt(0)
	v_pk_mul_f32 v[148:149], v[148:149], s[10:11] op_sel_hi:[1,0]
	v_pk_mul_f32 v[150:151], v[150:151], s[10:11] op_sel_hi:[1,0]
	ds_write_b32 v103, v148 offset:7392
	ds_write_b32 v103, v149 offset:7396
	ds_write_b32 v103, v150 offset:7400
	ds_write_b32 v103, v151 offset:7404
	s_waitcnt lgkmcnt(0)
	v_add_u32_e32 v12, 0x400, v7
	ds_read2_b32 v[22:23], v7 offset1:16
	ds_read2_b32 v[34:35], v7 offset0:33 offset1:49
	ds_read2_b32 v[38:39], v7 offset0:66 offset1:82
	ds_read2_b32 v[40:41], v7 offset0:99 offset1:115
	ds_read2_b32 v[42:43], v7 offset0:132 offset1:148
	ds_read2_b32 v[44:45], v7 offset0:165 offset1:181
	ds_read2_b32 v[46:47], v7 offset0:198 offset1:214
	ds_read2_b32 v[48:49], v7 offset0:231 offset1:247
	ds_read2_b32 v[50:51], v12 offset0:8 offset1:24
	ds_read2_b32 v[52:53], v12 offset0:41 offset1:57
	ds_read2_b32 v[54:55], v12 offset0:74 offset1:90
	ds_read2_b32 v[56:57], v12 offset0:107 offset1:123
	ds_read2_b32 v[58:59], v12 offset0:140 offset1:156
	ds_read2_b32 v[60:61], v12 offset0:173 offset1:189
	s_add_u32 s4, s1, s4
	v_mov_b32_e32 v30, v13
	v_mov_b32_e32 v31, v13
	v_mov_b32_e32 v32, v13
	ds_read2_b32 v[62:63], v12 offset0:206 offset1:222
	ds_read2_b32 v[64:65], v12 offset0:239 offset1:255
	v_mov_b32_e32 v33, v13
	s_addc_u32 s5, s2, s5
	s_lshl_b32 s7, s20, 4
	s_waitcnt lgkmcnt(14)
	v_cvt_pk_fp8_f32 v30, v22, v34
	s_waitcnt lgkmcnt(10)
	v_cvt_pk_fp8_f32 v31, v42, v44
	s_waitcnt lgkmcnt(6)
	v_cvt_pk_fp8_f32 v32, v50, v52
	s_waitcnt lgkmcnt(2)
	v_cvt_pk_fp8_f32 v33, v58, v60
	s_and_b32 s6, s21, 0x300
	s_and_b32 s20, s7, 0x60
	s_add_u32 s4, s4, s8
	v_or_b32_e32 v3, s6, v9
	s_addc_u32 s5, s5, 0
	v_or_b32_e32 v3, s20, v3
	v_lshl_add_u64 v[18:19], s[4:5], 0, v[10:11]
	s_and_b32 s4, s7, 16
	v_cvt_pk_fp8_f32 v30, v38, v40 op_sel:[0,0,1]
	v_cvt_pk_fp8_f32 v31, v46, v48 op_sel:[0,0,1]
	v_cvt_pk_fp8_f32 v32, v54, v56 op_sel:[0,0,1]
	s_waitcnt lgkmcnt(0)
	v_cvt_pk_fp8_f32 v33, v62, v64 op_sel:[0,0,1]
	v_or_b32_e32 v12, s4, v3
	v_lshlrev_b32_e32 v12, 10, v12
	v_lshl_add_u64 v[66:67], v[18:19], 0, v[12:13]
	global_store_dwordx4 v[66:67], v[30:33], off
	v_add_u32_e32 v3, s4, v3
	v_lshl_add_u32 v12, v3, 10, v29
	v_mov_b32_e32 v30, v13
	v_mov_b32_e32 v31, v13
	v_mov_b32_e32 v32, v13
	v_mov_b32_e32 v33, v13
	v_cvt_pk_fp8_f32 v30, v23, v35
	v_cvt_pk_fp8_f32 v31, v43, v45
	v_cvt_pk_fp8_f32 v32, v51, v53
	v_cvt_pk_fp8_f32 v33, v59, v61
	v_cvt_pk_fp8_f32 v30, v39, v41 op_sel:[0,0,1]
	v_cvt_pk_fp8_f32 v31, v47, v49 op_sel:[0,0,1]
	v_cvt_pk_fp8_f32 v32, v55, v57 op_sel:[0,0,1]
	v_cvt_pk_fp8_f32 v33, v63, v65 op_sel:[0,0,1]
	v_lshl_add_u64 v[18:19], v[18:19], 0, v[12:13]
	s_mov_b64 s[4:5], 0
	global_store_dwordx4 v[18:19], v[30:33], off
	s_waitcnt lgkmcnt(0)

.LBB0_20:
	v_readfirstlane_b32 s56, v18
	v_readfirstlane_b32 s57, v19
	s_lshl_b32 s51, s6, 13
	s_add_u32 s56, s56, s51
	s_addc_u32 s57, s57, 0
	s_lshl_b32 s52, s6, 2
	s_add_u32 s52, s4, s52
	s_addc_u32 s53, s5, 0
	v_and_b32_e32 v100, 3, v36
	v_lshrrev_b32_e32 v101, 5, v36
	v_lshl_or_b32 v100, v101, 2, v100
	v_bfe_u32 v101, v36, 2, 3
	v_lshlrev_b32_e32 v102, 13, v100
	v_lshl_or_b32 v102, v101, 4, v102
	v_lshlrev_b32_e32 v104, 2, v100
	v_lshlrev_b32_e32 v103, 2, v6
	v_sub_u32_e32 v103, v8, v103
	v_mad_u32_u24 v103, v100, s15, v103
	v_lshl_add_u32 v103, v101, 4, v103
	global_load_dwordx4 v[120:123], v102, s[56:57]
	s_add_u32 s56, s56, 0x10000
	s_addc_u32 s57, s57, 0
	global_load_dwordx4 v[124:127], v102, s[56:57]
	s_add_u32 s56, s56, 0x10000
	s_addc_u32 s57, s57, 0
	global_load_dword v152, v104, s[52:53] offset:0
	global_load_dword v153, v104, s[52:53] offset:32
	s_waitcnt vmcnt(1)
	v_pk_mul_f32 v[120:121], v[120:121], s[10:11] op_sel_hi:[1,0]
	v_pk_mul_f32 v[122:123], v[122:123], s[10:11] op_sel_hi:[1,0]
	v_mul_f32_e32 v120, v120, v152
	v_mul_f32_e32 v121, v121, v152
	v_mul_f32_e32 v122, v122, v152
	v_mul_f32_e32 v123, v123, v152
	ds_write_b32 v103, v120 offset:0
	ds_write_b32 v103, v121 offset:4
	ds_write_b32 v103, v122 offset:8
	ds_write_b32 v103, v123 offset:12
	s_waitcnt vmcnt(0)
	v_pk_mul_f32 v[124:125], v[124:125], s[10:11] op_sel_hi:[1,0]
	v_pk_mul_f32 v[126:127], v[126:127], s[10:11] op_sel_hi:[1,0]
	v_mul_f32_e32 v124, v124, v153
	v_mul_f32_e32 v125, v125, v153
	v_mul_f32_e32 v126, v126, v153
	v_mul_f32_e32 v127, v127, v153
	ds_write_b32 v103, v124 offset:1056
	ds_write_b32 v103, v125 offset:1060
	ds_write_b32 v103, v126 offset:1064
	ds_write_b32 v103, v127 offset:1068
	global_load_dwordx4 v[128:131], v102, s[56:57]
	s_add_u32 s56, s56, 0x10000
	s_addc_u32 s57, s57, 0
	global_load_dwordx4 v[132:135], v102, s[56:57]
	s_add_u32 s56, s56, 0x10000
	s_addc_u32 s57, s57, 0
	global_load_dword v154, v104, s[52:53] offset:64
	global_load_dword v155, v104, s[52:53] offset:96
	s_waitcnt vmcnt(1)
	v_pk_mul_f32 v[128:129], v[128:129], s[10:11] op_sel_hi:[1,0]
	v_pk_mul_f32 v[130:131], v[130:131], s[10:11] op_sel_hi:[1,0]
	v_mul_f32_e32 v128, v128, v154
	v_mul_f32_e32 v129, v129, v154
	v_mul_f32_e32 v130, v130, v154
	v_mul_f32_e32 v131, v131, v154
	ds_write_b32 v103, v128 offset:2112
	ds_write_b32 v103, v129 offset:2116
	ds_write_b32 v103, v130 offset:2120
	ds_write_b32 v103, v131 offset:2124
	s_waitcnt vmcnt(0)
	v_pk_mul_f32 v[132:133], v[132:133], s[10:11] op_sel_hi:[1,0]
	v_pk_mul_f32 v[134:135], v[134:135], s[10:11] op_sel_hi:[1,0]
	v_mul_f32_e32 v132, v132, v155
	v_mul_f32_e32 v133, v133, v155
	v_mul_f32_e32 v134, v134, v155
	v_mul_f32_e32 v135, v135, v155
	ds_write_b32 v103, v132 offset:3168
	ds_write_b32 v103, v133 offset:3172
	ds_write_b32 v103, v134 offset:3176
	ds_write_b32 v103, v135 offset:3180
	global_load_dwordx4 v[136:139], v102, s[56:57]
	s_add_u32 s56, s56, 0x10000
	s_addc_u32 s57, s57, 0
	global_load_dwordx4 v[140:143], v102, s[56:57]
	s_add_u32 s56, s56, 0x10000
	s_addc_u32 s57, s57, 0
	global_load_dword v156, v104, s[52:53] offset:128
	global_load_dword v157, v104, s[52:53] offset:160
	s_waitcnt vmcnt(1)
	v_pk_mul_f32 v[136:137], v[136:137], s[10:11] op_sel_hi:[1,0]
	v_pk_mul_f32 v[138:139], v[138:139], s[10:11] op_sel_hi:[1,0]
	v_mul_f32_e32 v136, v136, v156
	v_mul_f32_e32 v137, v137, v156
	v_mul_f32_e32 v138, v138, v156
	v_mul_f32_e32 v139, v139, v156
	ds_write_b32 v103, v136 offset:4224
	ds_write_b32 v103, v137 offset:4228
	ds_write_b32 v103, v138 offset:4232
	ds_write_b32 v103, v139 offset:4236
	s_waitcnt vmcnt(0)
	v_pk_mul_f32 v[140:141], v[140:141], s[10:11] op_sel_hi:[1,0]
	v_pk_mul_f32 v[142:143], v[142:143], s[10:11] op_sel_hi:[1,0]
	v_mul_f32_e32 v140, v140, v157
	v_mul_f32_e32 v141, v141, v157
	v_mul_f32_e32 v142, v142, v157
	v_mul_f32_e32 v143, v143, v157
	ds_write_b32 v103, v140 offset:5280
	ds_write_b32 v103, v141 offset:5284
	ds_write_b32 v103, v142 offset:5288
	ds_write_b32 v103, v143 offset:5292
	global_load_dwordx4 v[144:147], v102, s[56:57]
	s_add_u32 s56, s56, 0x10000
	s_addc_u32 s57, s57, 0
	global_load_dwordx4 v[148:151], v102, s[56:57]
	s_add_u32 s56, s56, 0x10000
	s_addc_u32 s57, s57, 0
	global_load_dword v158, v104, s[52:53] offset:192
	global_load_dword v159, v104, s[52:53] offset:224
	s_waitcnt vmcnt(1)
	v_pk_mul_f32 v[144:145], v[144:145], s[10:11] op_sel_hi:[1,0]
	v_pk_mul_f32 v[146:147], v[146:147], s[10:11] op_sel_hi:[1,0]
	v_mul_f32_e32 v144, v144, v158
	v_mul_f32_e32 v145, v145, v158
	v_mul_f32_e32 v146, v146, v158
	v_mul_f32_e32 v147, v147, v158
	ds_write_b32 v103, v144 offset:6336
	ds_write_b32 v103, v145 offset:6340
	ds_write_b32 v103, v146 offset:6344
	ds_write_b32 v103, v147 offset:6348
	s_waitcnt vmcnt(0)
	v_pk_mul_f32 v[148:149], v[148:149], s[10:11] op_sel_hi:[1,0]
	v_pk_mul_f32 v[150:151], v[150:151], s[10:11] op_sel_hi:[1,0]
	v_mul_f32_e32 v148, v148, v159
	v_mul_f32_e32 v149, v149, v159
	v_mul_f32_e32 v150, v150, v159
	v_mul_f32_e32 v151, v151, v159
	ds_write_b32 v103, v148 offset:7392
	ds_write_b32 v103, v149 offset:7396
	ds_write_b32 v103, v150 offset:7400
	ds_write_b32 v103, v151 offset:7404
	s_waitcnt lgkmcnt(0)
	v_add_u32_e32 v12, 0x400, v7
	ds_read2_b32 v[22:23], v7 offset1:16
	ds_read2_b32 v[34:35], v7 offset0:33 offset1:49
	ds_read2_b32 v[38:39], v7 offset0:66 offset1:82
	ds_read2_b32 v[40:41], v7 offset0:99 offset1:115
	ds_read2_b32 v[42:43], v7 offset0:132 offset1:148
	ds_read2_b32 v[44:45], v7 offset0:165 offset1:181
	ds_read2_b32 v[46:47], v7 offset0:198 offset1:214
	ds_read2_b32 v[48:49], v7 offset0:231 offset1:247
	ds_read2_b32 v[50:51], v12 offset0:8 offset1:24
	ds_read2_b32 v[52:53], v12 offset0:41 offset1:57
	ds_read2_b32 v[54:55], v12 offset0:74 offset1:90
	ds_read2_b32 v[56:57], v12 offset0:107 offset1:123
	ds_read2_b32 v[58:59], v12 offset0:140 offset1:156
	ds_read2_b32 v[60:61], v12 offset0:173 offset1:189
	s_lshl_b64 s[4:5], s[8:9], 21
	v_mov_b32_e32 v30, v13
	v_mov_b32_e32 v31, v13
	v_mov_b32_e32 v32, v13
	ds_read2_b32 v[62:63], v12 offset0:206 offset1:222
	ds_read2_b32 v[64:65], v12 offset0:239 offset1:255
	v_mov_b32_e32 v33, v13
	s_add_u32 s4, s3, s4
	s_waitcnt lgkmcnt(14)
	v_cvt_pk_fp8_f32 v30, v22, v34
	s_waitcnt lgkmcnt(10)
	v_cvt_pk_fp8_f32 v31, v42, v44
	s_waitcnt lgkmcnt(6)
	v_cvt_pk_fp8_f32 v32, v50, v52
	s_waitcnt lgkmcnt(2)
	v_cvt_pk_fp8_f32 v33, v58, v60
	s_addc_u32 s5, s11, s5
	s_lshl_b32 s8, s20, 6
	s_lshl_b32 s20, s20, 2
	s_and_b32 s8, s8, 0x700
	s_and_b32 s20, s20, 0x80
	s_or_b32 s8, s8, s20
	s_and_b32 s7, s7, 0x60
	s_add_u32 s4, s4, s6
	v_or_b32_e32 v3, s7, v5
	v_cvt_pk_fp8_f32 v30, v38, v40 op_sel:[0,0,1]
	v_cvt_pk_fp8_f32 v31, v46, v48 op_sel:[0,0,1]
	v_cvt_pk_fp8_f32 v32, v54, v56 op_sel:[0,0,1]
	s_waitcnt lgkmcnt(0)
	v_cvt_pk_fp8_f32 v33, v62, v64 op_sel:[0,0,1]
	s_addc_u32 s5, s5, 0
	v_or_b32_e32 v3, s8, v3
	v_lshl_add_u64 v[18:19], s[4:5], 0, v[10:11]
	v_lshlrev_b32_e32 v12, 10, v3
	v_lshl_add_u64 v[66:67], v[18:19], 0, v[12:13]
	global_store_dwordx4 v[66:67], v[30:33], off
	v_or_b32_e32 v3, s7, v21
	v_or_b32_e32 v3, s8, v3
	v_mov_b32_e32 v30, v13
	v_mov_b32_e32 v31, v13
	v_mov_b32_e32 v32, v13
	v_mov_b32_e32 v33, v13
	v_cvt_pk_fp8_f32 v30, v23, v35
	v_cvt_pk_fp8_f32 v31, v43, v45
	v_cvt_pk_fp8_f32 v32, v51, v53
	v_cvt_pk_fp8_f32 v33, v59, v61
	v_cvt_pk_fp8_f32 v30, v39, v41 op_sel:[0,0,1]
	v_cvt_pk_fp8_f32 v31, v47, v49 op_sel:[0,0,1]
	v_cvt_pk_fp8_f32 v32, v55, v57 op_sel:[0,0,1]
	v_cvt_pk_fp8_f32 v33, v63, v65 op_sel:[0,0,1]
	v_lshlrev_b32_e32 v12, 10, v3
	v_lshl_add_u64 v[18:19], v[18:19], 0, v[12:13]
	global_store_dwordx4 v[18:19], v[30:33], off
	s_waitcnt lgkmcnt(0)
